# in-proj epilogue: the line-contiguous bf16 output stores carry the nt (streaming) hint
# speedup vs baseline: 1.0109x; 1.0109x over previous
; #define LAS __attribute__((address_space(3)))
; __device__ __forceinline__ unsigned cvt_pk_bf16(float lo, float hi) { unsigned r; asm volatile("v_cvt_pk_bf16_f32 %0, %1, %2" : "=v"(r) : "v"(lo), "v"(hi)); return r; }
;     __device__ __forceinline__ void operator()(const f32x4 (&acc)[2][2][4][2], const Unit& u, int wr, int wc, int fr, int fq, const LAS unsigned* rt) const {
;         const float sc = INV_IN8 * ((u.pn < 2) ? 0.125f : ((u.pn == 8 || u.pn == 9) ? 0.08838834764831845f : 1.f));
;         const int row0 = u.pm * BM + wr * 64 + fr, col0 = u.pn * BM + wc * 64 + 16 * fq;
; #pragma unroll
;         for (int ai = 0; ai < 2; ++ai)
; #pragma unroll
;             for (int m = 0; m < 4; ++m) { bf16_t* rowp = O + (size_t)(row0 + ai * HALF + m * 16) * DIN + col0;
; #pragma unroll
;                 for (int bj = 0; bj < 2; ++bj) { const f32x4 v0 = acc[ai][bj][m][0] * sc, v1 = acc[ai][bj][m][1] * sc;
;                     u32x4 w; w.x = cvt_pk_bf16(v0[0], v0[1]); w.y = cvt_pk_bf16(v0[2], v0[3]); w.z = cvt_pk_bf16(v1[0], v1[1]); w.w = cvt_pk_bf16(v1[2], v1[3]);
;                     *(u32x4*)(rowp + 8 * bj) = w; } }
.LBB0_210:
	s_and_b32 s4, s52, -2
	s_cmp_eq_u32 s4, 8
	s_cselect_b64 vcc, -1, 0
	s_cmp_gt_i32 s52, 1
	v_mbcnt_lo_u32_b32 v16, -1, 0
	v_mbcnt_hi_u32_b32 v16, -1, v16
	v_and_b32_e32 v17, 7, v16
	v_lshrrev_b32_e32 v18, 3, v16
	v_and_b32_e32 v26, 0xffffffc0, v184
	v_lshl_or_b32 v26, v17, 3, v26
	v_and_b32_e32 v27, 0xffffffc0, v183
	v_or_b32_e32 v27, v27, v18
	v_lshrrev_b32_e32 v19, 6, v183
	v_lshrrev_b32_e32 v21, 6, v184
	v_lshl_add_u32 v19, v19, 2, v21
	v_mul_u32_u24_e32 v19, 0x900, v19
	v_add_u32_e32 v19, 0x20000, v19
	v_and_b32_e32 v21, 15, v183
	v_mul_u32_u24_e32 v21, 0x90, v21
	v_bfe_u32 v23, v184, 4, 2
	v_lshl_add_u32 v21, v23, 5, v21
	v_add_u32_e32 v21, v21, v19
	v_mul_u32_u24_e32 v23, 0x90, v18
	v_lshl_add_u32 v23, v17, 4, v23
	v_add_u32_e32 v23, v23, v19
	v_mov_b32_e32 v16, 0xe000
	v_mov_b32_e32 v17, 0
	v_lshl_add_u32 v4, s52, 8, v26
	v_cndmask_b32_e32 v0, v186, v187, vcc
	s_cselect_b64 vcc, -1, 0
	v_lshl_add_u32 v1, s28, 8, v27
	v_ashrrev_i32_e32 v5, 31, v4
	v_mov_b64_e32 v[2:3], s[16:17]
	v_cndmask_b32_e32 v0, v188, v0, vcc
	v_mad_i64_i32 v[6:7], s[4:5], v1, s51, v[2:3]
	v_lshlrev_b64 v[4:5], 1, v[4:5]
	s_nop 15
	s_nop 15
	v_lshl_add_u64 v[10:11], v[6:7], 0, v[4:5]
	v_pk_mul_f32 v[6:7], v[0:1], v[152:153] op_sel_hi:[0,1]
	v_pk_mul_f32 v[8:9], v[0:1], v[154:155] op_sel_hi:[0,1]
	v_cvt_pk_bf16_f32 v6, v6, v7
	v_cvt_pk_bf16_f32 v7, v8, v9
	v_pk_mul_f32 v[12:13], v[0:1], v[150:151] op_sel_hi:[0,1]
	v_pk_mul_f32 v[14:15], v[0:1], v[148:149] op_sel_hi:[0,1]
	v_cvt_pk_bf16_f32 v8, v14, v15
	v_cvt_pk_bf16_f32 v9, v12, v13
	v_mov_b64_e32 v[204:205], v[10:11]
	v_lshl_add_u64 v[208:209], v[10:11], 0, v[16:17]
	ds_write_b128 v21, v[6:9]
	v_pk_mul_f32 v[12:13], v[0:1], v[142:143] op_sel_hi:[0,1]
	v_pk_mul_f32 v[14:15], v[0:1], v[140:141] op_sel_hi:[0,1]
	v_pk_mul_f32 v[6:7], v[0:1], v[144:145] op_sel_hi:[0,1]
	v_pk_mul_f32 v[8:9], v[0:1], v[146:147] op_sel_hi:[0,1]
	v_cvt_pk_bf16_f32 v6, v6, v7
	v_cvt_pk_bf16_f32 v7, v8, v9
	v_cvt_pk_bf16_f32 v8, v14, v15
	v_cvt_pk_bf16_f32 v9, v12, v13
	ds_write_b128 v21, v[6:9] offset:16
	ds_read_b128 v[192:195], v23
	ds_read_b128 v[196:199], v23 offset:1152
	v_pk_mul_f32 v[12:13], v[0:1], v[134:135] op_sel_hi:[0,1]
	v_pk_mul_f32 v[14:15], v[0:1], v[132:133] op_sel_hi:[0,1]
	v_or_b32_e32 v6, 16, v1
	v_mad_i64_i32 v[6:7], s[4:5], v6, s51, v[2:3]
	v_lshl_add_u64 v[10:11], v[6:7], 0, v[4:5]
	v_pk_mul_f32 v[6:7], v[0:1], v[136:137] op_sel_hi:[0,1]
	v_pk_mul_f32 v[8:9], v[0:1], v[138:139] op_sel_hi:[0,1]
	v_cvt_pk_bf16_f32 v6, v6, v7
	v_cvt_pk_bf16_f32 v7, v8, v9
	v_cvt_pk_bf16_f32 v8, v14, v15
	v_cvt_pk_bf16_f32 v9, v12, v13
	v_mov_b64_e32 v[206:207], v[10:11]
	v_lshl_add_u64 v[210:211], v[10:11], 0, v[16:17]
	ds_write_b128 v21, v[6:9]
	v_pk_mul_f32 v[12:13], v[0:1], v[126:127] op_sel_hi:[0,1]
	v_pk_mul_f32 v[14:15], v[0:1], v[124:125] op_sel_hi:[0,1]
	v_pk_mul_f32 v[6:7], v[0:1], v[128:129] op_sel_hi:[0,1]
	v_pk_mul_f32 v[8:9], v[0:1], v[130:131] op_sel_hi:[0,1]
	v_cvt_pk_bf16_f32 v6, v6, v7
	v_cvt_pk_bf16_f32 v7, v8, v9
	v_cvt_pk_bf16_f32 v8, v14, v15
	v_cvt_pk_bf16_f32 v9, v12, v13
	s_waitcnt lgkmcnt(1)
	global_store_dwordx4 v[204:205], v[192:195], off nt
	global_store_dwordx4 v[208:209], v[196:199], off nt
	ds_write_b128 v21, v[6:9] offset:16
	ds_read_b128 v[192:195], v23
	ds_read_b128 v[196:199], v23 offset:1152
	v_pk_mul_f32 v[12:13], v[0:1], v[118:119] op_sel_hi:[0,1]
	v_pk_mul_f32 v[14:15], v[0:1], v[116:117] op_sel_hi:[0,1]
	v_or_b32_e32 v6, 32, v1
	v_mad_i64_i32 v[6:7], s[4:5], v6, s51, v[2:3]
	v_lshl_add_u64 v[10:11], v[6:7], 0, v[4:5]
	v_pk_mul_f32 v[6:7], v[0:1], v[120:121] op_sel_hi:[0,1]
	v_pk_mul_f32 v[8:9], v[0:1], v[122:123] op_sel_hi:[0,1]
	v_cvt_pk_bf16_f32 v6, v6, v7
	v_cvt_pk_bf16_f32 v7, v8, v9
	v_cvt_pk_bf16_f32 v8, v14, v15
	v_cvt_pk_bf16_f32 v9, v12, v13
	v_mov_b64_e32 v[204:205], v[10:11]
	v_lshl_add_u64 v[208:209], v[10:11], 0, v[16:17]
	ds_write_b128 v21, v[6:9]
	v_pk_mul_f32 v[12:13], v[0:1], v[110:111] op_sel_hi:[0,1]
	v_pk_mul_f32 v[14:15], v[0:1], v[108:109] op_sel_hi:[0,1]
	v_pk_mul_f32 v[6:7], v[0:1], v[112:113] op_sel_hi:[0,1]
	v_pk_mul_f32 v[8:9], v[0:1], v[114:115] op_sel_hi:[0,1]
	v_cvt_pk_bf16_f32 v6, v6, v7
	v_cvt_pk_bf16_f32 v7, v8, v9
	v_cvt_pk_bf16_f32 v8, v14, v15
	v_cvt_pk_bf16_f32 v9, v12, v13
	s_waitcnt lgkmcnt(1)
	global_store_dwordx4 v[206:207], v[192:195], off nt
	global_store_dwordx4 v[210:211], v[196:199], off nt
	ds_write_b128 v21, v[6:9] offset:16
	ds_read_b128 v[192:195], v23
	ds_read_b128 v[196:199], v23 offset:1152
	v_pk_mul_f32 v[12:13], v[0:1], v[98:99] op_sel_hi:[0,1]
	v_pk_mul_f32 v[14:15], v[0:1], v[96:97] op_sel_hi:[0,1]
	v_or_b32_e32 v6, 48, v1
	v_mad_i64_i32 v[6:7], s[4:5], v6, s51, v[2:3]
	v_lshl_add_u64 v[10:11], v[6:7], 0, v[4:5]
	v_pk_mul_f32 v[6:7], v[0:1], v[104:105] op_sel_hi:[0,1]
	v_pk_mul_f32 v[8:9], v[0:1], v[106:107] op_sel_hi:[0,1]
	v_cvt_pk_bf16_f32 v6, v6, v7
	v_cvt_pk_bf16_f32 v7, v8, v9
	v_cvt_pk_bf16_f32 v8, v14, v15
	v_cvt_pk_bf16_f32 v9, v12, v13
	v_mov_b64_e32 v[206:207], v[10:11]
	v_lshl_add_u64 v[210:211], v[10:11], 0, v[16:17]
	ds_write_b128 v21, v[6:9]
	v_pk_mul_f32 v[12:13], v[0:1], v[90:91] op_sel_hi:[0,1]
	v_pk_mul_f32 v[14:15], v[0:1], v[88:89] op_sel_hi:[0,1]
	v_pk_mul_f32 v[6:7], v[0:1], v[92:93] op_sel_hi:[0,1]
	v_pk_mul_f32 v[8:9], v[0:1], v[94:95] op_sel_hi:[0,1]
	v_cvt_pk_bf16_f32 v6, v6, v7
	v_cvt_pk_bf16_f32 v7, v8, v9
	v_cvt_pk_bf16_f32 v8, v14, v15
	v_cvt_pk_bf16_f32 v9, v12, v13
	s_waitcnt lgkmcnt(1)
; __device__ __forceinline__ unsigned cvt_pk_bf16(float lo, float hi) { unsigned r; asm volatile("v_cvt_pk_bf16_f32 %0, %1, %2" : "=v"(r) : "v"(lo), "v"(hi)); return r; }
;     __device__ __forceinline__ void operator()(const f32x4 (&acc)[2][2][4][2], const Unit& u, int wr, int wc, int fr, int fq, const LAS unsigned* rt) const {
;     ...
;             for (int m = 0; m < 4; ++m) { bf16_t* rowp = O + (size_t)(row0 + ai * HALF + m * 16) * DIN + col0;
; #pragma unroll
;                 for (int bj = 0; bj < 2; ++bj) { const f32x4 v0 = acc[ai][bj][m][0] * sc, v1 = acc[ai][bj][m][1] * sc;
;                     u32x4 w; w.x = cvt_pk_bf16(v0[0], v0[1]); w.y = cvt_pk_bf16(v0[2], v0[3]); w.z = cvt_pk_bf16(v1[0], v1[1]); w.w = cvt_pk_bf16(v1[2], v1[3]);
;                     *(u32x4*)(rowp + 8 * bj) = w; } }
	global_store_dwordx4 v[204:205], v[192:195], off nt
	global_store_dwordx4 v[208:209], v[196:199], off nt
	ds_write_b128 v21, v[6:9] offset:16
	ds_read_b128 v[192:195], v23
	ds_read_b128 v[196:199], v23 offset:1152
	v_pk_mul_f32 v[12:13], v[0:1], v[82:83] op_sel_hi:[0,1]
	v_pk_mul_f32 v[14:15], v[0:1], v[80:81] op_sel_hi:[0,1]
	v_add_u32_e32 v6, 0x80, v1
	v_mad_i64_i32 v[6:7], s[4:5], v6, s51, v[2:3]
	v_lshl_add_u64 v[10:11], v[6:7], 0, v[4:5]
	v_pk_mul_f32 v[6:7], v[0:1], v[84:85] op_sel_hi:[0,1]
	v_pk_mul_f32 v[8:9], v[0:1], v[86:87] op_sel_hi:[0,1]
	v_cvt_pk_bf16_f32 v6, v6, v7
	v_cvt_pk_bf16_f32 v7, v8, v9
	v_cvt_pk_bf16_f32 v8, v14, v15
	v_cvt_pk_bf16_f32 v9, v12, v13
	v_mov_b64_e32 v[204:205], v[10:11]
	v_lshl_add_u64 v[208:209], v[10:11], 0, v[16:17]
	ds_write_b128 v21, v[6:9]
	v_pk_mul_f32 v[12:13], v[0:1], v[102:103] op_sel_hi:[0,1]
	v_pk_mul_f32 v[14:15], v[0:1], v[100:101] op_sel_hi:[0,1]
	v_pk_mul_f32 v[6:7], v[0:1], v[76:77] op_sel_hi:[0,1]
	v_pk_mul_f32 v[8:9], v[0:1], v[78:79] op_sel_hi:[0,1]
	v_cvt_pk_bf16_f32 v6, v6, v7
	v_cvt_pk_bf16_f32 v7, v8, v9
	v_cvt_pk_bf16_f32 v8, v14, v15
	v_cvt_pk_bf16_f32 v9, v12, v13
	s_waitcnt lgkmcnt(1)
	global_store_dwordx4 v[206:207], v[192:195], off nt
	global_store_dwordx4 v[210:211], v[196:199], off nt
	ds_write_b128 v21, v[6:9] offset:16
	ds_read_b128 v[192:195], v23
	ds_read_b128 v[196:199], v23 offset:1152
	v_pk_mul_f32 v[12:13], v[0:1], v[62:63] op_sel_hi:[0,1]
	v_pk_mul_f32 v[14:15], v[0:1], v[60:61] op_sel_hi:[0,1]
	v_add_u32_e32 v6, 0x90, v1
	v_mad_i64_i32 v[6:7], s[4:5], v6, s51, v[2:3]
	v_lshl_add_u64 v[10:11], v[6:7], 0, v[4:5]
	v_pk_mul_f32 v[6:7], v[0:1], v[64:65] op_sel_hi:[0,1]
	v_pk_mul_f32 v[8:9], v[0:1], v[66:67] op_sel_hi:[0,1]
	v_cvt_pk_bf16_f32 v6, v6, v7
	v_cvt_pk_bf16_f32 v7, v8, v9
	v_cvt_pk_bf16_f32 v8, v14, v15
	v_cvt_pk_bf16_f32 v9, v12, v13
	v_mov_b64_e32 v[206:207], v[10:11]
	v_lshl_add_u64 v[210:211], v[10:11], 0, v[16:17]
	ds_write_b128 v21, v[6:9]
	v_pk_mul_f32 v[12:13], v[0:1], v[70:71] op_sel_hi:[0,1]
	v_pk_mul_f32 v[14:15], v[0:1], v[68:69] op_sel_hi:[0,1]
	v_pk_mul_f32 v[6:7], v[0:1], v[72:73] op_sel_hi:[0,1]
	v_pk_mul_f32 v[8:9], v[0:1], v[74:75] op_sel_hi:[0,1]
	v_cvt_pk_bf16_f32 v6, v6, v7
	v_cvt_pk_bf16_f32 v7, v8, v9
	v_cvt_pk_bf16_f32 v8, v14, v15
	v_cvt_pk_bf16_f32 v9, v12, v13
	s_waitcnt lgkmcnt(1)
	global_store_dwordx4 v[204:205], v[192:195], off nt
	global_store_dwordx4 v[208:209], v[196:199], off nt
	ds_write_b128 v21, v[6:9] offset:16
	ds_read_b128 v[192:195], v23
	ds_read_b128 v[196:199], v23 offset:1152
	v_pk_mul_f32 v[12:13], v[0:1], v[46:47] op_sel_hi:[0,1]
	v_pk_mul_f32 v[14:15], v[0:1], v[44:45] op_sel_hi:[0,1]
	v_add_u32_e32 v6, 0xa0, v1
	v_mad_i64_i32 v[6:7], s[4:5], v6, s51, v[2:3]
	v_lshl_add_u64 v[10:11], v[6:7], 0, v[4:5]
	v_pk_mul_f32 v[8:9], v[0:1], v[50:51] op_sel_hi:[0,1]
	v_pk_mul_f32 v[6:7], v[0:1], v[48:49] op_sel_hi:[0,1]
	v_cvt_pk_bf16_f32 v6, v6, v7
	v_cvt_pk_bf16_f32 v7, v8, v9
	v_cvt_pk_bf16_f32 v8, v14, v15
	v_cvt_pk_bf16_f32 v9, v12, v13
	v_mov_b64_e32 v[204:205], v[10:11]
	v_lshl_add_u64 v[208:209], v[10:11], 0, v[16:17]
	ds_write_b128 v21, v[6:9]
	v_pk_mul_f32 v[12:13], v[0:1], v[54:55] op_sel_hi:[0,1]
	v_pk_mul_f32 v[14:15], v[0:1], v[52:53] op_sel_hi:[0,1]
	v_pk_mul_f32 v[8:9], v[0:1], v[58:59] op_sel_hi:[0,1]
	v_pk_mul_f32 v[6:7], v[0:1], v[56:57] op_sel_hi:[0,1]
	v_add_u32_e32 v1, 0xb0, v1
	v_cvt_pk_bf16_f32 v6, v6, v7
	v_cvt_pk_bf16_f32 v7, v8, v9
	v_mad_i64_i32 v[2:3], s[4:5], v1, s51, v[2:3]
	v_cvt_pk_bf16_f32 v8, v14, v15
	v_cvt_pk_bf16_f32 v9, v12, v13
	s_waitcnt lgkmcnt(1)
	global_store_dwordx4 v[206:207], v[192:195], off nt
	global_store_dwordx4 v[210:211], v[196:199], off nt
	ds_write_b128 v21, v[6:9] offset:16
	ds_read_b128 v[192:195], v23
	ds_read_b128 v[196:199], v23 offset:1152
	v_pk_mul_f32 v[10:11], v[0:1], v[32:33] op_sel_hi:[0,1]
	s_andn2_b64 vcc, exec, s[6:7]
	v_lshl_add_u64 v[6:7], v[2:3], 0, v[4:5]
	v_pk_mul_f32 v[2:3], v[0:1], v[36:37] op_sel_hi:[0,1]
	v_pk_mul_f32 v[4:5], v[0:1], v[38:39] op_sel_hi:[0,1]
	v_cvt_pk_bf16_f32 v2, v2, v3
	v_cvt_pk_bf16_f32 v3, v4, v5
	v_pk_mul_f32 v[8:9], v[0:1], v[34:35] op_sel_hi:[0,1]
	v_cvt_pk_bf16_f32 v4, v10, v11
	v_cvt_pk_bf16_f32 v5, v8, v9
	v_mov_b64_e32 v[206:207], v[6:7]
	v_lshl_add_u64 v[210:211], v[6:7], 0, v[16:17]
	ds_write_b128 v21, v[2:5]
	s_mov_b64 s[4:5], -1
	v_pk_mul_f32 v[8:9], v[0:1], v[30:31] op_sel_hi:[0,1]
	v_pk_mul_f32 v[2:3], v[0:1], v[42:43] op_sel_hi:[0,1]
	v_pk_mul_f32 v[4:5], v[0:1], v[40:41] op_sel_hi:[0,1]
	v_pk_mul_f32 v[10:11], v[0:1], v[28:29] op_sel_hi:[0,1]
	v_cvt_pk_bf16_f32 v0, v4, v5
	v_cvt_pk_bf16_f32 v1, v2, v3
	v_cvt_pk_bf16_f32 v2, v10, v11
	v_cvt_pk_bf16_f32 v3, v8, v9
	s_waitcnt lgkmcnt(1)
	global_store_dwordx4 v[204:205], v[192:195], off nt
	global_store_dwordx4 v[208:209], v[196:199], off nt
	ds_write_b128 v21, v[0:3] offset:16
	ds_read_b128 v[192:195], v23
	ds_read_b128 v[196:199], v23 offset:1152
	s_waitcnt lgkmcnt(0)
	global_store_dwordx4 v[206:207], v[192:195], off nt
	global_store_dwordx4 v[210:211], v[196:199], off nt
	s_cbranch_vccnz .LBB0_203
	s_andn2_b64 vcc, exec, s[12:13]
	s_cbranch_vccnz .LBB0_202
	s_barrier
	s_branch .LBB0_202
